# baseline (speedup 1.0000x reference)
.Lmk_nomax:
	v_sub_f32_e32 v34, v34, v195
	v_fmamk_f32 v34, v34, 0x3fb8aa3b, v187
	v_exp_f32_e32 v34, v34
	s_nop 0
	v_cvt_f16_f32_e32 v34, v34
	v_cndmask_b32_e64 v34, 0, v34, s[56:57]
	ds_write_b16 v115, v34
	ds_read_b64_tr_b16 v[200:201], v193 offset:0
	ds_read_b64_tr_b16 v[202:203], v193 offset:512
	ds_read_b64_tr_b16 v[160:161], v193 offset:1024
	ds_read_b64_tr_b16 v[162:163], v193 offset:1536
	s_and_b64 vcc, exec, s[54:55]
	s_cbranch_vccnz .Lmk_first_path
	s_waitcnt vmcnt(0)
	ds_write_b16 v115, v35
	ds_write_b128 v196, v[10:13]
	ds_write_b128 v196, v[14:17] offset:1024
	ds_write_b128 v196, v[30:33] offset:2048
	ds_write_b128 v196, v[26:29] offset:3072
	s_cmp_lt_i32 s30, 33
	s_cbranch_scc1 .Lmk_lo_only
	ds_write_b128 v196, v[2:5] offset:4096
	ds_write_b128 v196, v[6:9] offset:5120
	ds_write_b128 v196, v[18:21] offset:6144
	ds_write_b128 v196, v[22:25] offset:7168
	s_waitcnt lgkmcnt(9)
	v_mfma_f32_16x16x32_f16 v[54:57], v[130:133], v[200:203], v[54:57]
	v_mfma_f32_16x16x32_f16 v[58:61], v[134:137], v[200:203], v[58:61]
	v_mfma_f32_16x16x32_f16 v[62:65], v[138:141], v[200:203], v[62:65]
	v_mfma_f32_16x16x32_f16 v[66:69], v[142:145], v[200:203], v[66:69]
	v_mfma_f32_16x16x32_f16 v[70:73], v[168:171], v[200:203], v[70:73]

.Lmk_first_path:
	s_waitcnt vmcnt(8)
	s_waitcnt lgkmcnt(0)
	v_mfma_f32_16x16x32_f16 v[54:57], v[130:133], v[200:203], 0
	ds_write_b16 v115, v35
	ds_write_b128 v196, v[10:13]
	v_mfma_f32_16x16x32_f16 v[58:61], v[134:137], v[200:203], 0
	ds_write_b128 v196, v[14:17] offset:1024
	v_mfma_f32_16x16x32_f16 v[62:65], v[138:141], v[200:203], 0
	ds_write_b128 v196, v[30:33] offset:2048
	v_mfma_f32_16x16x32_f16 v[66:69], v[142:145], v[200:203], 0
	ds_write_b128 v196, v[26:29] offset:3072
	v_mfma_f32_16x16x32_f16 v[70:73], v[168:171], v[200:203], 0
	s_cmp_lt_i32 s30, 33
	s_cbranch_scc1 .Lmk_st_done
	ds_write_b128 v196, v[2:5] offset:4096
	ds_write_b128 v196, v[6:9] offset:5120
	ds_write_b128 v196, v[18:21] offset:6144
	ds_write_b128 v196, v[22:25] offset:7168
	s_branch .Lmk_st_done
.Lmk_lo_only:
	s_waitcnt lgkmcnt(5)
	v_mfma_f32_16x16x32_f16 v[54:57], v[130:133], v[200:203], v[54:57]
	v_mfma_f32_16x16x32_f16 v[58:61], v[134:137], v[200:203], v[58:61]
	v_mfma_f32_16x16x32_f16 v[62:65], v[138:141], v[200:203], v[62:65]
	v_mfma_f32_16x16x32_f16 v[66:69], v[142:145], v[200:203], v[66:69]
	v_mfma_f32_16x16x32_f16 v[70:73], v[168:171], v[200:203], v[70:73]
	s_branch .Lmk_st_done
